# step-major attention conversion order + half-staggered job buffer (rows 0-3 at step start, rows 4-7 at step end, low halves relayed through LDS)
# baseline (speedup 1.0000x reference)
; __device__ __forceinline__ unsigned pk4_fp8_scaled(float a, float b, float c, float d) { s16x2 r = {0, 0}; r = __builtin_amdgcn_cvt_scalef32_pk_fp8_f32(r, a, b, pg8::W8_INV, false); r = __builtin_amdgcn_cvt_scalef32_pk_fp8_f32(r, c, d, pg8::W8_INV, true); return __builtin_bit_cast(unsigned, r); }
; __device__ __forceinline__ SJob sjob_addr(const Args& a, int j, int lane) {
;     SJob c; const int kseg = lane & 7, nq = lane >> 3;
;     if (j < SJOBS_GU) { const int e = j >> 12, kb = (j >> 7) & 31, nb = j & 127, s0 = nb * 32, bj = s0 >> 11, rem = s0 & 2047, pn = rem >> 7, c0 = rem & 127, np = pn * 256 + bj * 128 + c0;
;         c.ld = 4096; c.src = a.w_gate_up + ((size_t)e * 2048 + kb * 64 + kseg * 8) * 4096 + s0 + nq * 4; c.dst = (unsigned char*)(a.ws + WS_WGU_T) + ((size_t)e * 4096 + np + nq * 4) * 2048 + kb * 64 + kseg * 8; }
;     else { const int jj = j - SJOBS_GU, e = jj >> 11, kb = (jj >> 6) & 31, nb = jj & 63;
;         c.ld = 2048; c.src = a.w_down + ((size_t)e * 2048 + kb * 64 + kseg * 8) * 2048 + nb * 32 + nq * 4; c.dst = (unsigned char*)(a.ws + WS_WD_T) + ((size_t)e * 2048 + nb * 32 + nq * 4) * 2048 + kb * 64 + kseg * 8; }
;     return c;
; }
; __device__ __forceinline__ void sjob_load(const SJob& c, f32x4 (&v)[8]) {
; #pragma unroll
;     for (int r = 0; r < 8; ++r) v[r] = __builtin_nontemporal_load((const f32x4*)(c.src + (size_t)r * c.ld));
; }
; __device__ __forceinline__ void sjob_store(const SJob& c, const f32x4 (&v)[8]) {
; #pragma unroll
;     for (int jn = 0; jn < 4; ++jn) { u32x2 o;
;         o.x = pk4_fp8_scaled(v[0][jn], v[1][jn], v[2][jn], v[3][jn]); o.y = pk4_fp8_scaled(v[4][jn], v[5][jn], v[6][jn], v[7][jn]);
;         __builtin_nontemporal_store(o, (u32x2*)(c.dst + (size_t)jn * 2048)); }
; }
; __device__ __forceinline__ void moba_attn_unit(const Args& a, LAS unsigned char* lds, int bh, int qb, int half, int cjob0) {
;     ...
;         if (CONV_IN_ATTN) { { const SJob cj = sjob_addr(a, cjob + 8 * s, lane); sjob_store(cj, cv); } if (s + 1 < nsteps) { const SJob cn = sjob_addr(a, cjob + 8 * (s + 1), lane); sjob_load(cn, cv); } }
.LBB0_436:
	s_or_b64 exec, exec, s[16:17]
	s_cmp_lt_u32 s59, s53
	s_cbranch_scc1 .Lh1a_w16
	s_waitcnt vmcnt(0)
	s_branch .Lh1a_wd
.Lh1a_w16:
	s_waitcnt vmcnt(12)
.Lh1a_wd:
	v_lshlrev_b32_e32 v131, 2, v0
	v_add_u32_e32 v131, 0x20400, v131
	ds_read_b32 v132, v131
	ds_read_b32 v134, v131 offset:2048
	ds_read_b32 v136, v131 offset:4096
	ds_read_b32 v138, v131 offset:6144
	s_lshr_b32 s8, s1, 12
	s_bfe_u32 s9, s1, 0x50007
	s_and_b32 s10, s1, 0x7f
	s_bfe_u32 s11, s10, 0x40002
	s_lshl_b32 s11, s11, 8
	s_lshr_b32 s16, s10, 6
	s_lshl_b32 s16, s16, 7
	s_add_i32 s11, s11, s16
	s_and_b32 s16, s10, 3
	s_lshl_b32 s16, s16, 5
	s_add_i32 s11, s11, s16
	s_lshl_b32 s16, s8, 23
	s_lshl_b32 s11, s11, 11
	s_add_u32 s16, s16, s11
	s_lshl_b32 s11, s9, 6
	s_add_u32 s16, s16, s11
	s_add_u32 s16, s16, 0xb300000
	s_add_u32 s16, s74, s16
	s_addc_u32 s17, s75, 0
	v_lshlrev_b32_e32 v130, 11, v180
	v_add_u32_e32 v130, v130, v178
	v_cvt_scalef32_pk_fp8_f32 v133, v114, v118, s23
	v_cvt_scalef32_pk_fp8_f32 v135, v115, v119, s23
	v_cvt_scalef32_pk_fp8_f32 v137, v116, v120, s23
	v_cvt_scalef32_pk_fp8_f32 v139, v117, v121, s23
	v_cvt_scalef32_pk_fp8_f32 v133, v122, v126, s23 op_sel:[0,0,0,1]
	v_cvt_scalef32_pk_fp8_f32 v135, v123, v127, s23 op_sel:[0,0,0,1]
	v_cvt_scalef32_pk_fp8_f32 v137, v124, v128, s23 op_sel:[0,0,0,1]
	v_cvt_scalef32_pk_fp8_f32 v139, v125, v129, s23 op_sel:[0,0,0,1]
	s_waitcnt lgkmcnt(0)
	global_store_dwordx2 v130, v[132:133], s[16:17] nt
	global_store_dwordx2 v130, v[134:135], s[16:17] offset:2048 nt
	s_add_u32 s16, s16, 0x1000
	s_addc_u32 s17, s17, 0
	global_store_dwordx2 v130, v[136:137], s[16:17] nt
	global_store_dwordx2 v130, v[138:139], s[16:17] offset:2048 nt
	s_cmp_lt_u32 s59, s53
	s_cbranch_scc0 .Lh1a_done
	s_add_i32 s8, s1, 0x800
	s_lshr_b32 s9, s8, 12
	s_bfe_u32 s10, s8, 0x50007
	s_and_b32 s11, s8, 0x7f
	s_lshl_b32 s9, s9, 25
	s_lshl_b32 s10, s10, 20
	s_add_u32 s9, s9, s10
	s_lshl_b32 s11, s11, 7
	s_add_u32 s9, s9, s11
	s_add_u32 s9, s9, 0x10000
	s_add_u32 s18, s46, s9
	s_addc_u32 s19, s47, 0
	v_lshlrev_b32_e32 v140, 14, v178
	v_add_u32_e32 v140, v140, v168
	global_load_dwordx4 v[114:117], v140, s[18:19] nt
	s_add_u32 s18, s18, 0x4000
	s_addc_u32 s19, s19, 0
	global_load_dwordx4 v[118:121], v140, s[18:19] nt
	s_add_u32 s18, s18, 0x4000
	s_addc_u32 s19, s19, 0
	global_load_dwordx4 v[122:125], v140, s[18:19] nt
	s_add_u32 s18, s18, 0x4000
	s_addc_u32 s19, s19, 0
	global_load_dwordx4 v[126:129], v140, s[18:19] nt
.Lh1a_done:
	s_add_i32 s56, s56, 0x10000
	s_add_i32 s58, s58, 2
	s_add_i32 s1, s1, 0x800
	s_add_i32 s31, s31, 0x10000
	s_add_i32 s55, s55, 0x20000
	s_cmp_eq_u32 s53, s59
	s_cbranch_scc1 .LBB0_462
.LBB0_437:
	s_cmp_eq_u32 s59, 0
	s_cbranch_scc1 .Lhsa_full
	s_waitcnt vmcnt(8)
	s_branch .Lhsa_j

; __device__ __forceinline__ void moba_attn_unit(const Args& a, LAS unsigned char* lds, int bh, int qb, int half, int cjob0) {
;     ...
;     for (int s = 0; s < nsteps; ++s) {
;         asm volatile("s_waitcnt vmcnt(0)" ::: "memory");
;         __syncthreads();
;         if (s + 1 < nsteps) stage(s + 1);
;         if (CONV_IN_ATTN) { { const SJob cj = sjob_addr(a, cjob + 8 * s, lane); sjob_store(cj, cv); } if (s + 1 < nsteps) { const SJob cn = sjob_addr(a, cjob + 8 * (s + 1), lane); sjob_load(cn, cv); } }
.Lhsa_j:
	s_add_i32 s59, s59, 1
	s_cmp_lt_u32 s59, s53
	s_cselect_b64 s[8:9], -1, 0
	s_cmp_ge_u32 s59, s53
	s_waitcnt lgkmcnt(0)
	s_barrier
	s_cbranch_scc0 .LBB0_460
	s_cmp_gt_i32 s1, 0x1ffff
	s_mov_b64 s[16:17], -1
	s_cbranch_scc1 .LBB0_461

; __device__ __forceinline__ unsigned pk4_fp8_scaled(float a, float b, float c, float d) { s16x2 r = {0, 0}; r = __builtin_amdgcn_cvt_scalef32_pk_fp8_f32(r, a, b, pg8::W8_INV, false); r = __builtin_amdgcn_cvt_scalef32_pk_fp8_f32(r, c, d, pg8::W8_INV, true); return __builtin_bit_cast(unsigned, r); }
; __device__ __forceinline__ void sjob_store(const SJob& c, const f32x4 (&v)[8]) {
; #pragma unroll
;     for (int jn = 0; jn < 4; ++jn) { u32x2 o;
;         o.x = pk4_fp8_scaled(v[0][jn], v[1][jn], v[2][jn], v[3][jn]); o.y = pk4_fp8_scaled(v[4][jn], v[5][jn], v[6][jn], v[7][jn]);
;         __builtin_nontemporal_store(o, (u32x2*)(c.dst + (size_t)jn * 2048)); }
; }
.LBB0_441:
	s_add_u32 s10, s74, s10
	s_addc_u32 s11, s75, s11
	v_lshlrev_b64 v[130:131], 11, v[130:131]
	s_and_b32 s12, s12, 0x7c0
	v_lshl_add_u64 v[130:131], s[10:11], 0, v[130:131]
	v_mov_b32_e32 v132, 0
	v_lshl_add_u64 v[130:131], v[130:131], 0, s[12:13]
	v_cvt_scalef32_pk_fp8_f32 v132, v98, v102, s23
	v_lshl_add_u64 v[130:131], v[130:131], 0, v[178:179]
	v_cvt_scalef32_pk_fp8_f32 v132, v106, v110, s23 op_sel:[0,0,0,1]
	v_lshlrev_b32_e32 v133, 2, v0
	v_add_u32_e32 v133, 0x20400, v133
	ds_write_b32 v133, v132
	v_mov_b32_e32 v132, 0
	v_cvt_scalef32_pk_fp8_f32 v132, v99, v103, s23
	v_cvt_scalef32_pk_fp8_f32 v132, v107, v111, s23 op_sel:[0,0,0,1]
	ds_write_b32 v133, v132 offset:2048
	v_mov_b32_e32 v132, 0
	v_cvt_scalef32_pk_fp8_f32 v132, v100, v104, s23
	v_add_co_u32_e32 v130, vcc, 0x1000, v130
	v_cvt_scalef32_pk_fp8_f32 v132, v108, v112, s23 op_sel:[0,0,0,1]
	v_addc_co_u32_e32 v131, vcc, 0, v131, vcc
	ds_write_b32 v133, v132 offset:4096
	v_mov_b32_e32 v132, 0
	v_cvt_scalef32_pk_fp8_f32 v132, v101, v105, s23
	v_cvt_scalef32_pk_fp8_f32 v132, v109, v113, s23 op_sel:[0,0,0,1]
	s_andn2_b64 vcc, exec, s[8:9]
	ds_write_b32 v133, v132 offset:6144
	s_cbranch_vccnz .LBB0_447
	s_add_i32 s10, s1, 0x800
	s_cmp_gt_i32 s10, 0x1ffff
	s_mov_b64 s[8:9], -1
	s_cbranch_scc0 .LBB0_444
	s_and_b32 s2, s10, 0x7fffffc0
	s_add_i32 s2, s2, 0xfffe0000
	v_or_b32_e32 v98, s2, v178
	v_mov_b32_e32 v99, v169
	v_lshlrev_b64 v[98:99], 13, v[98:99]
	s_add_i32 s2, s31, 0x10000
	v_lshl_add_u64 v[98:99], s[50:51], 0, v[98:99]
	s_and_b32 s12, s2, 0x7e0
	s_mov_b64 s[8:9], 0

; __device__ __forceinline__ void sjob_load(const SJob& c, f32x4 (&v)[8]) {
; #pragma unroll
;     for (int r = 0; r < 8; ++r) v[r] = __builtin_nontemporal_load((const f32x4*)(c.src + (size_t)r * c.ld));
; }
.LBB0_446:
	v_lshl_add_u64 v[98:99], s[12:13], 2, v[98:99]
	v_lshl_add_u64 v[98:99], v[98:99], 0, v[168:169]
	s_lshl_b32 s12, s8, 2
	v_lshl_add_u64 v[106:107], v[98:99], 0, s[12:13]
	global_load_dwordx4 v[98:101], v[98:99], off nt
	s_nop 0
	global_load_dwordx4 v[102:105], v[106:107], off nt
	v_lshl_add_u64 v[106:107], v[106:107], 0, s[12:13]
	v_lshl_add_u64 v[134:135], v[106:107], 0, s[12:13]
	global_load_dwordx4 v[106:109], v[106:107], off nt
	s_nop 0
	global_load_dwordx4 v[110:113], v[134:135], off nt

; __device__ __forceinline__ void moba_attn_unit(const Args& a, LAS unsigned char* lds, int bh, int qb, int half, int cjob0) {
;     ...
;     for (int s = 0; s < nsteps; ++s) {
;         asm volatile("s_waitcnt vmcnt(0)" ::: "memory");
;         __syncthreads();
;         if (s + 1 < nsteps) stage(s + 1);
;         if (CONV_IN_ATTN) { { const SJob cj = sjob_addr(a, cjob + 8 * s, lane); sjob_store(cj, cv); } if (s + 1 < nsteps) { const SJob cn = sjob_addr(a, cjob + 8 * (s + 1), lane); sjob_load(cn, cv); } }
.LBB0_473:
	s_or_b64 exec, exec, s[16:17]
	s_cmp_lt_i32 s58, s52
	s_cbranch_scc1 .Lh1b_w16
	s_waitcnt vmcnt(0)
	s_branch .Lh1b_wd

; __device__ __forceinline__ unsigned pk4_fp8_scaled(float a, float b, float c, float d) { s16x2 r = {0, 0}; r = __builtin_amdgcn_cvt_scalef32_pk_fp8_f32(r, a, b, pg8::W8_INV, false); r = __builtin_amdgcn_cvt_scalef32_pk_fp8_f32(r, c, d, pg8::W8_INV, true); return __builtin_bit_cast(unsigned, r); }
; __device__ __forceinline__ SJob sjob_addr(const Args& a, int j, int lane) {
;     SJob c; const int kseg = lane & 7, nq = lane >> 3;
;     if (j < SJOBS_GU) { const int e = j >> 12, kb = (j >> 7) & 31, nb = j & 127, s0 = nb * 32, bj = s0 >> 11, rem = s0 & 2047, pn = rem >> 7, c0 = rem & 127, np = pn * 256 + bj * 128 + c0;
;         c.ld = 4096; c.src = a.w_gate_up + ((size_t)e * 2048 + kb * 64 + kseg * 8) * 4096 + s0 + nq * 4; c.dst = (unsigned char*)(a.ws + WS_WGU_T) + ((size_t)e * 4096 + np + nq * 4) * 2048 + kb * 64 + kseg * 8; }
;     else { const int jj = j - SJOBS_GU, e = jj >> 11, kb = (jj >> 6) & 31, nb = jj & 63;
;         c.ld = 2048; c.src = a.w_down + ((size_t)e * 2048 + kb * 64 + kseg * 8) * 2048 + nb * 32 + nq * 4; c.dst = (unsigned char*)(a.ws + WS_WD_T) + ((size_t)e * 2048 + nb * 32 + nq * 4) * 2048 + kb * 64 + kseg * 8; }
;     return c;
; }
; __device__ __forceinline__ void sjob_load(const SJob& c, f32x4 (&v)[8]) {
; #pragma unroll
;     for (int r = 0; r < 8; ++r) v[r] = __builtin_nontemporal_load((const f32x4*)(c.src + (size_t)r * c.ld));
; }
; __device__ __forceinline__ void sjob_store(const SJob& c, const f32x4 (&v)[8]) {
; #pragma unroll
;     for (int jn = 0; jn < 4; ++jn) { u32x2 o;
;         o.x = pk4_fp8_scaled(v[0][jn], v[1][jn], v[2][jn], v[3][jn]); o.y = pk4_fp8_scaled(v[4][jn], v[5][jn], v[6][jn], v[7][jn]);
;         __builtin_nontemporal_store(o, (u32x2*)(c.dst + (size_t)jn * 2048)); }
; }
.Lh1b_wd:
	v_lshlrev_b32_e32 v36, 2, v0
	v_add_u32_e32 v36, 0x20400, v36
	ds_read_b32 v134, v36
	ds_read_b32 v136, v36 offset:2048
	ds_read_b32 v138, v36 offset:4096
	ds_read_b32 v140, v36 offset:6144
	s_lshr_b32 s8, s1, 12
	s_bfe_u32 s9, s1, 0x50007
	s_and_b32 s10, s1, 0x7f
	s_bfe_u32 s11, s10, 0x40002
	s_lshl_b32 s11, s11, 8
	s_lshr_b32 s16, s10, 6
	s_lshl_b32 s16, s16, 7
	s_add_i32 s11, s11, s16
	s_and_b32 s16, s10, 3
	s_lshl_b32 s16, s16, 5
	s_add_i32 s11, s11, s16
	s_lshl_b32 s16, s8, 23
	s_lshl_b32 s11, s11, 11
	s_add_u32 s16, s16, s11
	s_lshl_b32 s11, s9, 6
	s_add_u32 s16, s16, s11
	s_add_u32 s16, s16, 0xb300000
	s_add_u32 s16, s74, s16
	s_addc_u32 s17, s75, 0
	v_lshlrev_b32_e32 v37, 11, v180
	v_add_u32_e32 v37, v37, v178
	v_cvt_scalef32_pk_fp8_f32 v135, v118, v122, s23
	v_cvt_scalef32_pk_fp8_f32 v137, v119, v123, s23
	v_cvt_scalef32_pk_fp8_f32 v139, v120, v124, s23
	v_cvt_scalef32_pk_fp8_f32 v141, v121, v125, s23
	v_cvt_scalef32_pk_fp8_f32 v135, v126, v130, s23 op_sel:[0,0,0,1]
	v_cvt_scalef32_pk_fp8_f32 v137, v127, v131, s23 op_sel:[0,0,0,1]
	v_cvt_scalef32_pk_fp8_f32 v139, v128, v132, s23 op_sel:[0,0,0,1]
	v_cvt_scalef32_pk_fp8_f32 v141, v129, v133, s23 op_sel:[0,0,0,1]
	s_waitcnt lgkmcnt(0)
	global_store_dwordx2 v37, v[134:135], s[16:17] nt
	global_store_dwordx2 v37, v[136:137], s[16:17] offset:2048 nt
	s_add_u32 s16, s16, 0x1000
	s_addc_u32 s17, s17, 0
	global_store_dwordx2 v37, v[138:139], s[16:17] nt
	global_store_dwordx2 v37, v[140:141], s[16:17] offset:2048 nt
	s_cmp_lt_i32 s58, s52
	s_cbranch_scc0 .Lh1b_done
	s_add_i32 s8, s1, 0x800
	s_lshr_b32 s9, s8, 12
	s_bfe_u32 s10, s8, 0x50007
	s_and_b32 s11, s8, 0x7f
	s_lshl_b32 s9, s9, 25
	s_lshl_b32 s10, s10, 20
	s_add_u32 s9, s9, s10
	s_lshl_b32 s11, s11, 7
	s_add_u32 s9, s9, s11
	s_add_u32 s9, s9, 0x10000
	s_add_u32 s18, s46, s9
	s_addc_u32 s19, s47, 0
	v_lshlrev_b32_e32 v36, 14, v178
	v_add_u32_e32 v36, v36, v168
	global_load_dwordx4 v[118:121], v36, s[18:19] nt
	s_add_u32 s18, s18, 0x4000
	s_addc_u32 s19, s19, 0
	global_load_dwordx4 v[122:125], v36, s[18:19] nt
	s_add_u32 s18, s18, 0x4000
	s_addc_u32 s19, s19, 0
	global_load_dwordx4 v[126:129], v36, s[18:19] nt
	s_add_u32 s18, s18, 0x4000
	s_addc_u32 s19, s19, 0
	global_load_dwordx4 v[130:133], v36, s[18:19] nt
.Lh1b_done:
	s_add_i32 s53, s53, 0x10000
	s_add_i32 s57, s57, 2
	s_add_i32 s1, s1, 0x800
	s_add_i32 s54, s54, 0x10000
	s_add_i32 s55, s55, 0x20000
	s_cmp_eq_u32 s52, s58
	s_cbranch_scc1 .LBB0_500
.LBB0_474:
	s_cmp_eq_u32 s58, 0
	s_cbranch_scc1 .Lhsb_full
	s_waitcnt vmcnt(8)
	s_branch .Lhsb_j

; __device__ __forceinline__ void moba_attn_unit(const Args& a, LAS unsigned char* lds, int bh, int qb, int half, int cjob0) {
;     ...
;     for (int s = 0; s < nsteps; ++s) {
;         asm volatile("s_waitcnt vmcnt(0)" ::: "memory");
;         __syncthreads();
;         if (s + 1 < nsteps) stage(s + 1);
;         if (CONV_IN_ATTN) { { const SJob cj = sjob_addr(a, cjob + 8 * s, lane); sjob_store(cj, cv); } if (s + 1 < nsteps) { const SJob cn = sjob_addr(a, cjob + 8 * (s + 1), lane); sjob_load(cn, cv); } }
.Lhsb_j:
	s_add_i32 s58, s58, 1
	s_cmp_lt_i32 s58, s52
	s_cselect_b64 s[8:9], -1, 0
	s_cmp_ge_i32 s58, s52
	s_waitcnt lgkmcnt(0)
	s_barrier
	s_cbranch_scc0 .LBB0_497
	s_cmp_gt_i32 s1, 0x1ffff
	s_mov_b64 s[16:17], -1
	s_cbranch_scc1 .LBB0_498

; __device__ __forceinline__ unsigned pk4_fp8_scaled(float a, float b, float c, float d) { s16x2 r = {0, 0}; r = __builtin_amdgcn_cvt_scalef32_pk_fp8_f32(r, a, b, pg8::W8_INV, false); r = __builtin_amdgcn_cvt_scalef32_pk_fp8_f32(r, c, d, pg8::W8_INV, true); return __builtin_bit_cast(unsigned, r); }
; __device__ __forceinline__ void sjob_store(const SJob& c, const f32x4 (&v)[8]) {
; #pragma unroll
;     for (int jn = 0; jn < 4; ++jn) { u32x2 o;
;         o.x = pk4_fp8_scaled(v[0][jn], v[1][jn], v[2][jn], v[3][jn]); o.y = pk4_fp8_scaled(v[4][jn], v[5][jn], v[6][jn], v[7][jn]);
;         __builtin_nontemporal_store(o, (u32x2*)(c.dst + (size_t)jn * 2048)); }
; }
.LBB0_478:
	s_add_u32 s10, s74, s10
	s_addc_u32 s11, s75, s11
	v_lshlrev_b64 v[36:37], 11, v[36:37]
	s_and_b32 s12, s12, 0x7c0
	v_lshl_add_u64 v[36:37], s[10:11], 0, v[36:37]
	v_mov_b32_e32 v134, 0
	v_lshl_add_u64 v[36:37], v[36:37], 0, s[12:13]
	v_cvt_scalef32_pk_fp8_f32 v134, v102, v106, s23
	v_lshl_add_u64 v[36:37], v[36:37], 0, v[178:179]
	v_cvt_scalef32_pk_fp8_f32 v134, v110, v114, s23 op_sel:[0,0,0,1]
	v_lshlrev_b32_e32 v135, 2, v0
	v_add_u32_e32 v135, 0x20400, v135
	ds_write_b32 v135, v134
	v_mov_b32_e32 v134, 0
	v_cvt_scalef32_pk_fp8_f32 v134, v103, v107, s23
	v_cvt_scalef32_pk_fp8_f32 v134, v111, v115, s23 op_sel:[0,0,0,1]
	ds_write_b32 v135, v134 offset:2048
	v_mov_b32_e32 v134, 0
	v_cvt_scalef32_pk_fp8_f32 v134, v104, v108, s23
	v_add_co_u32_e32 v36, vcc, 0x1000, v36
	v_cvt_scalef32_pk_fp8_f32 v134, v112, v116, s23 op_sel:[0,0,0,1]
	v_addc_co_u32_e32 v37, vcc, 0, v37, vcc
	ds_write_b32 v135, v134 offset:4096
	v_mov_b32_e32 v134, 0
	v_cvt_scalef32_pk_fp8_f32 v134, v105, v109, s23
	v_cvt_scalef32_pk_fp8_f32 v134, v113, v117, s23 op_sel:[0,0,0,1]
	s_andn2_b64 vcc, exec, s[8:9]
	ds_write_b32 v135, v134 offset:6144
	s_cbranch_vccnz .LBB0_484
	s_add_i32 s10, s1, 0x800
	s_cmp_gt_i32 s10, 0x1ffff
	s_mov_b64 s[8:9], -1
	s_cbranch_scc0 .LBB0_481
	s_and_b32 s2, s10, 0x7fffffc0
	s_add_i32 s2, s2, 0xfffe0000
	v_or_b32_e32 v36, s2, v178
	v_mov_b32_e32 v37, v169
	v_lshlrev_b64 v[36:37], 13, v[36:37]
	s_add_i32 s2, s54, 0x10000
	v_lshl_add_u64 v[36:37], s[50:51], 0, v[36:37]
	s_and_b32 s12, s2, 0x7e0
	s_mov_b64 s[8:9], 0

; __device__ __forceinline__ void sjob_load(const SJob& c, f32x4 (&v)[8]) {
; #pragma unroll
;     for (int r = 0; r < 8; ++r) v[r] = __builtin_nontemporal_load((const f32x4*)(c.src + (size_t)r * c.ld));
; }
.LBB0_483:
	v_lshl_add_u64 v[36:37], s[12:13], 2, v[36:37]
	v_lshl_add_u64 v[36:37], v[36:37], 0, v[168:169]
	s_lshl_b32 s12, s8, 2
	v_lshl_add_u64 v[110:111], v[36:37], 0, s[12:13]
	global_load_dwordx4 v[102:105], v[36:37], off nt
	global_load_dwordx4 v[106:109], v[110:111], off nt
	v_lshl_add_u64 v[36:37], v[110:111], 0, s[12:13]
	v_lshl_add_u64 v[136:137], v[36:37], 0, s[12:13]
	global_load_dwordx4 v[110:113], v[36:37], off nt
	global_load_dwordx4 v[114:117], v[136:137], off nt
